# kernel start: silu(c) staging loads batched (16 loads in flight instead of 16 serial load-drain-compute rounds)
# speedup vs baseline: 1.0211x; 1.0020x over previous
; #define LAS __attribute__((address_space(3)))
; __device__ __forceinline__ void p0_prologue(Frame& F) {
;     LAS float* cs = (LAS float*)(F.lds);
;     LAS float* part = (LAS float*)(F.lds + 32768);
;     const float* c = inp(F, 1);
;     for (int i = F.tid; i < 8 * 1024; i += 512) { const float v = c[i]; cs[i] = v / (1.0f + __expf(-v)); }
;     __syncthreads();
.LBB0_16:
	global_load_dword v100, v[2:3], off
	global_load_dword v101, v[2:3], off offset:2048
	v_lshl_add_u64 v[2:3], v[2:3], 0, s[6:7]
	v_lshl_add_u64 v[2:3], v[2:3], 0, s[6:7]
	global_load_dword v102, v[2:3], off
	global_load_dword v103, v[2:3], off offset:2048
	v_lshl_add_u64 v[2:3], v[2:3], 0, s[6:7]
	v_lshl_add_u64 v[2:3], v[2:3], 0, s[6:7]
	global_load_dword v104, v[2:3], off
	global_load_dword v105, v[2:3], off offset:2048
	v_lshl_add_u64 v[2:3], v[2:3], 0, s[6:7]
	v_lshl_add_u64 v[2:3], v[2:3], 0, s[6:7]
	global_load_dword v106, v[2:3], off
	global_load_dword v107, v[2:3], off offset:2048
	v_lshl_add_u64 v[2:3], v[2:3], 0, s[6:7]
	v_lshl_add_u64 v[2:3], v[2:3], 0, s[6:7]
	global_load_dword v108, v[2:3], off
	global_load_dword v109, v[2:3], off offset:2048
	v_lshl_add_u64 v[2:3], v[2:3], 0, s[6:7]
	v_lshl_add_u64 v[2:3], v[2:3], 0, s[6:7]
	global_load_dword v110, v[2:3], off
	global_load_dword v111, v[2:3], off offset:2048
	v_lshl_add_u64 v[2:3], v[2:3], 0, s[6:7]
	v_lshl_add_u64 v[2:3], v[2:3], 0, s[6:7]
	global_load_dword v112, v[2:3], off
	global_load_dword v113, v[2:3], off offset:2048
	v_lshl_add_u64 v[2:3], v[2:3], 0, s[6:7]
	v_lshl_add_u64 v[2:3], v[2:3], 0, s[6:7]
	global_load_dword v114, v[2:3], off
	global_load_dword v115, v[2:3], off offset:2048
	v_lshl_add_u64 v[2:3], v[2:3], 0, s[6:7]
	v_lshl_add_u64 v[2:3], v[2:3], 0, s[6:7]
	v_add_u32_e32 v4, 0x2000, v4
	s_waitcnt vmcnt(15)
	v_mul_f32_e32 v6, 0xbfb8aa3b, v100
	v_exp_f32_e32 v6, v6
	s_nop 0
	v_add_f32_e32 v6, 1.0, v6
	v_div_scale_f32 v7, s[10:11], v6, v6, v100
	v_rcp_f32_e32 v8, v7
	v_div_scale_f32 v9, vcc, v100, v6, v100
	v_fma_f32 v10, -v7, v8, 1.0
	v_fmac_f32_e32 v8, v10, v8
	v_mul_f32_e32 v10, v9, v8
	v_fma_f32 v11, -v7, v10, v9
	v_fmac_f32_e32 v10, v11, v8
	v_fma_f32 v7, -v7, v10, v9
	v_div_fmas_f32 v7, v7, v8, v10
	v_div_fixup_f32 v100, v7, v6, v100
	ds_write_b32 v1, v100
	s_waitcnt vmcnt(14)
	v_mul_f32_e32 v6, 0xbfb8aa3b, v101
	v_exp_f32_e32 v6, v6
	s_nop 0
	v_add_f32_e32 v6, 1.0, v6
	v_div_scale_f32 v7, s[10:11], v6, v6, v101
	v_rcp_f32_e32 v8, v7
	v_div_scale_f32 v9, vcc, v101, v6, v101
	v_fma_f32 v10, -v7, v8, 1.0
	v_fmac_f32_e32 v8, v10, v8
	v_mul_f32_e32 v10, v9, v8
	v_fma_f32 v11, -v7, v10, v9
	v_fmac_f32_e32 v10, v11, v8
	v_fma_f32 v7, -v7, v10, v9
	v_div_fmas_f32 v7, v7, v8, v10
	v_div_fixup_f32 v101, v7, v6, v101
	ds_write_b32 v1, v101 offset:2048
	s_waitcnt vmcnt(13)
	v_mul_f32_e32 v6, 0xbfb8aa3b, v102
	v_exp_f32_e32 v6, v6
	s_nop 0
	v_add_f32_e32 v6, 1.0, v6
	v_div_scale_f32 v7, s[10:11], v6, v6, v102
	v_rcp_f32_e32 v8, v7
	v_div_scale_f32 v9, vcc, v102, v6, v102
	v_fma_f32 v10, -v7, v8, 1.0
	v_fmac_f32_e32 v8, v10, v8
	v_mul_f32_e32 v10, v9, v8
	v_fma_f32 v11, -v7, v10, v9
	v_fmac_f32_e32 v10, v11, v8
	v_fma_f32 v7, -v7, v10, v9
	v_div_fmas_f32 v7, v7, v8, v10
	v_div_fixup_f32 v102, v7, v6, v102
	ds_write_b32 v1, v102 offset:4096
	s_waitcnt vmcnt(12)
	v_mul_f32_e32 v6, 0xbfb8aa3b, v103
	v_exp_f32_e32 v6, v6
	s_nop 0
	v_add_f32_e32 v6, 1.0, v6
	v_div_scale_f32 v7, s[10:11], v6, v6, v103
	v_rcp_f32_e32 v8, v7
	v_div_scale_f32 v9, vcc, v103, v6, v103
	v_fma_f32 v10, -v7, v8, 1.0
	v_fmac_f32_e32 v8, v10, v8
	v_mul_f32_e32 v10, v9, v8
	v_fma_f32 v11, -v7, v10, v9
	v_fmac_f32_e32 v10, v11, v8
	v_fma_f32 v7, -v7, v10, v9
	v_div_fmas_f32 v7, v7, v8, v10
	v_div_fixup_f32 v103, v7, v6, v103
	ds_write_b32 v1, v103 offset:6144
	s_waitcnt vmcnt(11)
	v_mul_f32_e32 v6, 0xbfb8aa3b, v104
	v_exp_f32_e32 v6, v6
	s_nop 0
	v_add_f32_e32 v6, 1.0, v6
	v_div_scale_f32 v7, s[10:11], v6, v6, v104
	v_rcp_f32_e32 v8, v7
	v_div_scale_f32 v9, vcc, v104, v6, v104
	v_fma_f32 v10, -v7, v8, 1.0
	v_fmac_f32_e32 v8, v10, v8
	v_mul_f32_e32 v10, v9, v8
	v_fma_f32 v11, -v7, v10, v9
	v_fmac_f32_e32 v10, v11, v8
	v_fma_f32 v7, -v7, v10, v9
	v_div_fmas_f32 v7, v7, v8, v10
	v_div_fixup_f32 v104, v7, v6, v104
	ds_write_b32 v1, v104 offset:8192
	s_waitcnt vmcnt(10)
	v_mul_f32_e32 v6, 0xbfb8aa3b, v105
	v_exp_f32_e32 v6, v6
	s_nop 0
	v_add_f32_e32 v6, 1.0, v6
	v_div_scale_f32 v7, s[10:11], v6, v6, v105
	v_rcp_f32_e32 v8, v7
	v_div_scale_f32 v9, vcc, v105, v6, v105
	v_fma_f32 v10, -v7, v8, 1.0
	v_fmac_f32_e32 v8, v10, v8
	v_mul_f32_e32 v10, v9, v8
	v_fma_f32 v11, -v7, v10, v9
	v_fmac_f32_e32 v10, v11, v8
	v_fma_f32 v7, -v7, v10, v9
	v_div_fmas_f32 v7, v7, v8, v10
	v_div_fixup_f32 v105, v7, v6, v105
	ds_write_b32 v1, v105 offset:10240
	s_waitcnt vmcnt(9)
	v_mul_f32_e32 v6, 0xbfb8aa3b, v106
	v_exp_f32_e32 v6, v6
	s_nop 0
	v_add_f32_e32 v6, 1.0, v6
	v_div_scale_f32 v7, s[10:11], v6, v6, v106
	v_rcp_f32_e32 v8, v7
	v_div_scale_f32 v9, vcc, v106, v6, v106
	v_fma_f32 v10, -v7, v8, 1.0
	v_fmac_f32_e32 v8, v10, v8
	v_mul_f32_e32 v10, v9, v8
	v_fma_f32 v11, -v7, v10, v9
	v_fmac_f32_e32 v10, v11, v8
	v_fma_f32 v7, -v7, v10, v9
	v_div_fmas_f32 v7, v7, v8, v10
	v_div_fixup_f32 v106, v7, v6, v106
	ds_write_b32 v1, v106 offset:12288
	s_waitcnt vmcnt(8)
; __device__ __forceinline__ void p0_prologue(Frame& F) {
;     ...
;     for (int i = F.tid; i < 8 * 1024; i += 512) { const float v = c[i]; cs[i] = v / (1.0f + __expf(-v)); }
;     __syncthreads();
;     float* mod = (float*)(F.ws + WS_MOD);
;     for (int it = F.vcu; it < 4 * 96; it += F.G) {
;         const int layer = it / 96, slab = it % 96; const int col = slab * 64 + F.lane;
;         const float* W = inp(F, 2) + (size_t)layer * 1024 * 6144 + col;
	v_mul_f32_e32 v6, 0xbfb8aa3b, v107
	v_exp_f32_e32 v6, v6
	s_nop 0
	v_add_f32_e32 v6, 1.0, v6
	v_div_scale_f32 v7, s[10:11], v6, v6, v107
	v_rcp_f32_e32 v8, v7
	v_div_scale_f32 v9, vcc, v107, v6, v107
	v_fma_f32 v10, -v7, v8, 1.0
	v_fmac_f32_e32 v8, v10, v8
	v_mul_f32_e32 v10, v9, v8
	v_fma_f32 v11, -v7, v10, v9
	v_fmac_f32_e32 v10, v11, v8
	v_fma_f32 v7, -v7, v10, v9
	v_div_fmas_f32 v7, v7, v8, v10
	v_div_fixup_f32 v107, v7, v6, v107
	ds_write_b32 v1, v107 offset:14336
	s_waitcnt vmcnt(7)
	v_mul_f32_e32 v6, 0xbfb8aa3b, v108
	v_exp_f32_e32 v6, v6
	s_nop 0
	v_add_f32_e32 v6, 1.0, v6
	v_div_scale_f32 v7, s[10:11], v6, v6, v108
	v_rcp_f32_e32 v8, v7
	v_div_scale_f32 v9, vcc, v108, v6, v108
	v_fma_f32 v10, -v7, v8, 1.0
	v_fmac_f32_e32 v8, v10, v8
	v_mul_f32_e32 v10, v9, v8
	v_fma_f32 v11, -v7, v10, v9
	v_fmac_f32_e32 v10, v11, v8
	v_fma_f32 v7, -v7, v10, v9
	v_div_fmas_f32 v7, v7, v8, v10
	v_div_fixup_f32 v108, v7, v6, v108
	ds_write_b32 v1, v108 offset:16384
	s_waitcnt vmcnt(6)
	v_mul_f32_e32 v6, 0xbfb8aa3b, v109
	v_exp_f32_e32 v6, v6
	s_nop 0
	v_add_f32_e32 v6, 1.0, v6
	v_div_scale_f32 v7, s[10:11], v6, v6, v109
	v_rcp_f32_e32 v8, v7
	v_div_scale_f32 v9, vcc, v109, v6, v109
	v_fma_f32 v10, -v7, v8, 1.0
	v_fmac_f32_e32 v8, v10, v8
	v_mul_f32_e32 v10, v9, v8
	v_fma_f32 v11, -v7, v10, v9
	v_fmac_f32_e32 v10, v11, v8
	v_fma_f32 v7, -v7, v10, v9
	v_div_fmas_f32 v7, v7, v8, v10
	v_div_fixup_f32 v109, v7, v6, v109
	ds_write_b32 v1, v109 offset:18432
	s_waitcnt vmcnt(5)
	v_mul_f32_e32 v6, 0xbfb8aa3b, v110
	v_exp_f32_e32 v6, v6
	s_nop 0
	v_add_f32_e32 v6, 1.0, v6
	v_div_scale_f32 v7, s[10:11], v6, v6, v110
	v_rcp_f32_e32 v8, v7
	v_div_scale_f32 v9, vcc, v110, v6, v110
	v_fma_f32 v10, -v7, v8, 1.0
	v_fmac_f32_e32 v8, v10, v8
	v_mul_f32_e32 v10, v9, v8
	v_fma_f32 v11, -v7, v10, v9
	v_fmac_f32_e32 v10, v11, v8
	v_fma_f32 v7, -v7, v10, v9
	v_div_fmas_f32 v7, v7, v8, v10
	v_div_fixup_f32 v110, v7, v6, v110
	ds_write_b32 v1, v110 offset:20480
	s_waitcnt vmcnt(4)
	v_mul_f32_e32 v6, 0xbfb8aa3b, v111
	v_exp_f32_e32 v6, v6
	s_nop 0
	v_add_f32_e32 v6, 1.0, v6
	v_div_scale_f32 v7, s[10:11], v6, v6, v111
	v_rcp_f32_e32 v8, v7
	v_div_scale_f32 v9, vcc, v111, v6, v111
	v_fma_f32 v10, -v7, v8, 1.0
	v_fmac_f32_e32 v8, v10, v8
	v_mul_f32_e32 v10, v9, v8
	v_fma_f32 v11, -v7, v10, v9
	v_fmac_f32_e32 v10, v11, v8
	v_fma_f32 v7, -v7, v10, v9
	v_div_fmas_f32 v7, v7, v8, v10
	v_div_fixup_f32 v111, v7, v6, v111
	ds_write_b32 v1, v111 offset:22528
	s_waitcnt vmcnt(3)
	v_mul_f32_e32 v6, 0xbfb8aa3b, v112
	v_exp_f32_e32 v6, v6
	s_nop 0
	v_add_f32_e32 v6, 1.0, v6
	v_div_scale_f32 v7, s[10:11], v6, v6, v112
	v_rcp_f32_e32 v8, v7
	v_div_scale_f32 v9, vcc, v112, v6, v112
	v_fma_f32 v10, -v7, v8, 1.0
	v_fmac_f32_e32 v8, v10, v8
	v_mul_f32_e32 v10, v9, v8
	v_fma_f32 v11, -v7, v10, v9
	v_fmac_f32_e32 v10, v11, v8
	v_fma_f32 v7, -v7, v10, v9
	v_div_fmas_f32 v7, v7, v8, v10
	v_div_fixup_f32 v112, v7, v6, v112
	ds_write_b32 v1, v112 offset:24576
	s_waitcnt vmcnt(2)
	v_mul_f32_e32 v6, 0xbfb8aa3b, v113
	v_exp_f32_e32 v6, v6
	s_nop 0
	v_add_f32_e32 v6, 1.0, v6
	v_div_scale_f32 v7, s[10:11], v6, v6, v113
	v_rcp_f32_e32 v8, v7
	v_div_scale_f32 v9, vcc, v113, v6, v113
	v_fma_f32 v10, -v7, v8, 1.0
	v_fmac_f32_e32 v8, v10, v8
	v_mul_f32_e32 v10, v9, v8
	v_fma_f32 v11, -v7, v10, v9
	v_fmac_f32_e32 v10, v11, v8
	v_fma_f32 v7, -v7, v10, v9
	v_div_fmas_f32 v7, v7, v8, v10
	v_div_fixup_f32 v113, v7, v6, v113
	ds_write_b32 v1, v113 offset:26624
	s_waitcnt vmcnt(1)
	v_mul_f32_e32 v6, 0xbfb8aa3b, v114
	v_exp_f32_e32 v6, v6
	s_nop 0
	v_add_f32_e32 v6, 1.0, v6
	v_div_scale_f32 v7, s[10:11], v6, v6, v114
	v_rcp_f32_e32 v8, v7
	v_div_scale_f32 v9, vcc, v114, v6, v114
	v_fma_f32 v10, -v7, v8, 1.0
	v_fmac_f32_e32 v8, v10, v8
	v_mul_f32_e32 v10, v9, v8
	v_fma_f32 v11, -v7, v10, v9
	v_fmac_f32_e32 v10, v11, v8
	v_fma_f32 v7, -v7, v10, v9
	v_div_fmas_f32 v7, v7, v8, v10
	v_div_fixup_f32 v114, v7, v6, v114
	ds_write_b32 v1, v114 offset:28672
	s_waitcnt vmcnt(0)
	v_mul_f32_e32 v6, 0xbfb8aa3b, v115
	v_exp_f32_e32 v6, v6
	s_nop 0
	v_add_f32_e32 v6, 1.0, v6
	v_div_scale_f32 v7, s[10:11], v6, v6, v115
	v_rcp_f32_e32 v8, v7
	v_div_scale_f32 v9, vcc, v115, v6, v115
	v_fma_f32 v10, -v7, v8, 1.0
	v_fmac_f32_e32 v8, v10, v8
	v_mul_f32_e32 v10, v9, v8
	v_fma_f32 v11, -v7, v10, v9
	v_fmac_f32_e32 v10, v11, v8
	v_fma_f32 v7, -v7, v10, v9
	v_div_fmas_f32 v7, v7, v8, v10
	v_div_fixup_f32 v115, v7, v6, v115
	ds_write_b32 v1, v115 offset:30720
	v_add_u32_e32 v1, 0x8000, v1
	s_or_b64 exec, exec, s[0:1]
	s_cmpk_gt_i32 s3, 0x17f
	s_waitcnt lgkmcnt(0)
	s_barrier
	s_cbranch_scc1 .LBB0_22
	s_lshl_b32 s0, s90, 11
	s_add_i32 s0, s0, 0
	v_lshlrev_b32_e32 v2, 2, v40
	v_add_u32_e32 v1, s0, v2
	s_lshl_b32 s0, s90, 7
	s_lshl_b32 s1, s90, 9
	s_add_i32 s10, s1, 0
	s_lshl_b32 s1, s90, 8
	s_mul_hi_u32 s12, s0, 0x6000
	s_mul_i32 s0, s90, 0x300000
	s_add_i32 s1, s1, 0
	s_or_b32 s13, s0, 0x30000
	s_add_i32 s0, 0, 0x21810
	v_add_u32_e32 v41, s1, v2
	s_movk_i32 s11, 0x6000
	v_mov_b32_e32 v42, s0
	s_mov_b32 s14, 0xfffe8000
	s_mov_b32 s15, 0xfffee000
	s_mov_b32 s18, 0xffff4000
	s_movk_i32 s19, 0xa000
	s_mov_b32 s22, 0xc000
	s_mov_b32 s23, 0x12000
	s_mov_b32 s24, 0x18000
	s_mov_b32 s25, 0x1e000
	s_mov_b32 s26, 0x24000
	s_mov_b32 s27, 0x2a000
	s_mov_b64 s[6:7], 0x60000
	s_add_i32 s28, 0, 0x21818
	s_mov_b32 s29, s3
